# diff attention tile loop: removed 32 dead v_mov zero-inits of the near-tile bias registers per tile
# speedup vs baseline: 1.0035x; 1.0035x over previous
; #define LAS __attribute__((address_space(3)))
; __device__ __forceinline__ void diff_tile(const bool near, const LAS unsigned char* Kb, const LAS unsigned char* Vb, const LAS float* btab, const LAS bf16x8* Qs, f32x16 (&O)[2][2],
;                                           float (&lsum)[2], int qpos, int k0, int l31, int hi, float c2, float farraw) {
;     float bm[2][16];
;     if (near) {
; #pragma unroll
;         for (int kb = 0; kb < 2; ++kb)
; #pragma unroll
;             for (int r = 0; r < 16; ++r) { const int dist = qpos - (k0 + 32 * kb + (r & 3) + 8 * (r >> 2) + 4 * hi); bm[kb][r] = btab[min(max(dist, 0), 128)]; }
; #pragma unroll
;         for (int kb = 0; kb < 2; ++kb)
; #pragma unroll
;             for (int r = 0; r < 16; ++r) { asm volatile("" : "+v"(bm[kb][r]));
;                 const int dist = qpos - (k0 + 32 * kb + (r & 3) + 8 * (r >> 2) + 4 * hi); bm[kb][r] = dist < 0 ? -INFINITY : (bm[kb][r] - farraw) * c2; }
;     ...
;             if (wave_on && k0 <= q0w + 31) {
;                 const LAS unsigned char* Kb = KV + cur * DF_KB; const LAS unsigned char* Vb = KV + (2 + cur) * DF_KB;
;                 diff_tile(q0w - (k0 + 63) < 113, Kb, Vb, btab + h * 132, Qs, O, lsum, qpos, k0, l31, hi, c2, farraw);
.LBB0_783:
	s_and_b32 s57, s56, 1
	s_cmp_le_i32 s51, s53
	s_cselect_b64 s[0:1], -1, 0
	s_and_b64 s[0:1], s[28:29], s[0:1]
	s_andn2_b64 vcc, exec, s[0:1]
	s_cbranch_vccnz .LBB0_791
	s_cmpk_lt_i32 s54, 0x71
	s_cselect_b64 s[38:39], -1, 0
	s_cmpk_gt_i32 s54, 0x70
	s_cbranch_scc1 .LBB0_786
	v_add_u32_e32 v96, s51, v186
	v_sub_u32_e32 v66, v149, v186
	v_add_u32_e32 v66, s54, v66
	v_or_b32_e32 v97, 3, v96
	v_or_b32_e32 v110, 2, v96
	v_or_b32_e32 v111, 9, v96
	v_or_b32_e32 v112, 8, v96
	v_or_b32_e32 v113, 11, v96
	v_or_b32_e32 v114, 10, v96
	v_or_b32_e32 v115, 17, v96
	v_or_b32_e32 v116, 16, v96
	v_or_b32_e32 v117, 19, v96
	v_or_b32_e32 v118, 18, v96
	v_or_b32_e32 v119, 25, v96
	v_or_b32_e32 v120, 24, v96
	v_or_b32_e32 v121, 27, v96
	v_or_b32_e32 v122, 26, v96
	v_or_b32_e32 v123, 33, v96
	v_or_b32_e32 v124, 32, v96
	v_or_b32_e32 v125, 35, v96
	v_or_b32_e32 v126, 34, v96
	v_or_b32_e32 v127, 41, v96
	v_or_b32_e32 v128, 40, v96
	v_or_b32_e32 v129, 43, v96
	v_or_b32_e32 v130, 42, v96
	v_or_b32_e32 v131, 49, v96
	v_or_b32_e32 v132, 48, v96
	v_or_b32_e32 v133, 51, v96
	v_or_b32_e32 v134, 50, v96
	v_or_b32_e32 v135, 57, v96
	v_or_b32_e32 v136, 56, v96
	v_add_u32_e32 v67, 63, v66
	v_add_u32_e32 v66, 62, v66
	v_sub_u32_e32 v68, v148, v110
	v_sub_u32_e32 v69, v148, v97
	v_sub_u32_e32 v70, v148, v112
	v_sub_u32_e32 v71, v148, v111
	v_sub_u32_e32 v72, v148, v114
	v_sub_u32_e32 v73, v148, v113
	v_sub_u32_e32 v74, v148, v116
	v_sub_u32_e32 v75, v148, v115
	v_sub_u32_e32 v76, v148, v118
	v_sub_u32_e32 v77, v148, v117
	v_sub_u32_e32 v78, v148, v120
	v_sub_u32_e32 v79, v148, v119
	v_sub_u32_e32 v80, v148, v122
	v_sub_u32_e32 v81, v148, v121
	v_sub_u32_e32 v82, v148, v124
	v_sub_u32_e32 v83, v148, v123
	v_sub_u32_e32 v84, v148, v126
	v_sub_u32_e32 v85, v148, v125
	v_sub_u32_e32 v86, v148, v128
	v_sub_u32_e32 v87, v148, v127
	v_sub_u32_e32 v88, v148, v130
	v_sub_u32_e32 v89, v148, v129
	v_sub_u32_e32 v90, v148, v132
	v_sub_u32_e32 v91, v148, v131
	v_sub_u32_e32 v92, v148, v134
	v_sub_u32_e32 v93, v148, v133
	v_sub_u32_e32 v94, v148, v136
	v_sub_u32_e32 v95, v148, v135
	v_or_b32_e32 v137, 59, v96
	v_or_b32_e32 v138, 58, v96
	v_med3_i32 v67, v67, 0, v218
	v_med3_i32 v66, v66, 0, v218
	v_med3_i32 v68, v68, 0, v218
	v_med3_i32 v69, v69, 0, v218
	v_med3_i32 v70, v70, 0, v218
	v_med3_i32 v71, v71, 0, v218
	v_med3_i32 v72, v72, 0, v218
	v_med3_i32 v73, v73, 0, v218
	v_med3_i32 v74, v74, 0, v218
	v_med3_i32 v75, v75, 0, v218
	v_med3_i32 v76, v76, 0, v218
	v_med3_i32 v77, v77, 0, v218
	v_med3_i32 v78, v78, 0, v218
	v_med3_i32 v79, v79, 0, v218
	v_med3_i32 v80, v80, 0, v218
	v_med3_i32 v81, v81, 0, v218
	v_med3_i32 v82, v82, 0, v218
	v_med3_i32 v83, v83, 0, v218
	v_med3_i32 v84, v84, 0, v218
	v_med3_i32 v85, v85, 0, v218
	v_med3_i32 v86, v86, 0, v218
	v_med3_i32 v87, v87, 0, v218
	v_med3_i32 v88, v88, 0, v218
	v_med3_i32 v89, v89, 0, v218
	v_med3_i32 v90, v90, 0, v218
	v_med3_i32 v91, v91, 0, v218
	v_med3_i32 v92, v92, 0, v218
	v_med3_i32 v93, v93, 0, v218
	v_med3_i32 v94, v94, 0, v218
	v_med3_i32 v95, v95, 0, v218
	v_sub_u32_e32 v139, v148, v138
	v_sub_u32_e32 v140, v148, v137
	v_lshl_add_u32 v67, v67, 2, s50
	v_lshl_add_u32 v66, v66, 2, s50
	v_lshl_add_u32 v68, v68, 2, s50
	v_lshl_add_u32 v69, v69, 2, s50
	v_lshl_add_u32 v70, v70, 2, s50
	v_lshl_add_u32 v71, v71, 2, s50
	v_lshl_add_u32 v72, v72, 2, s50
	v_lshl_add_u32 v73, v73, 2, s50
	v_lshl_add_u32 v74, v74, 2, s50
	v_lshl_add_u32 v75, v75, 2, s50
	v_lshl_add_u32 v76, v76, 2, s50
	v_lshl_add_u32 v77, v77, 2, s50
	v_lshl_add_u32 v78, v78, 2, s50
	v_lshl_add_u32 v79, v79, 2, s50
	v_lshl_add_u32 v80, v80, 2, s50
	v_lshl_add_u32 v81, v81, 2, s50
	v_lshl_add_u32 v82, v82, 2, s50
	v_lshl_add_u32 v83, v83, 2, s50
	v_lshl_add_u32 v84, v84, 2, s50
	v_lshl_add_u32 v85, v85, 2, s50
	v_lshl_add_u32 v86, v86, 2, s50
	v_lshl_add_u32 v87, v87, 2, s50
	v_lshl_add_u32 v88, v88, 2, s50
	v_lshl_add_u32 v89, v89, 2, s50
	v_lshl_add_u32 v90, v90, 2, s50
	v_lshl_add_u32 v91, v91, 2, s50
	v_lshl_add_u32 v92, v92, 2, s50
	v_lshl_add_u32 v93, v93, 2, s50
	v_lshl_add_u32 v94, v94, 2, s50
	v_lshl_add_u32 v95, v95, 2, s50
	v_med3_i32 v139, v139, 0, v218
	v_med3_i32 v140, v140, 0, v218
	v_lshl_add_u32 v139, v139, 2, s50
	v_lshl_add_u32 v140, v140, 2, s50
	ds_read_b32 v141, v67
	ds_read_b32 v152, v66
	ds_read_b32 v66, v68
	ds_read_b32 v67, v69
	ds_read_b32 v68, v70
	ds_read_b32 v69, v71
	ds_read_b32 v70, v72
	ds_read_b32 v71, v73
	ds_read_b32 v72, v74
	ds_read_b32 v73, v75
	ds_read_b32 v74, v76
	ds_read_b32 v75, v77
	ds_read_b32 v76, v78
	ds_read_b32 v77, v79
	ds_read_b32 v78, v80
	ds_read_b32 v79, v81
	ds_read_b32 v80, v82
	ds_read_b32 v81, v83
	ds_read_b32 v82, v84
	ds_read_b32 v83, v85
	ds_read_b32 v84, v86
	ds_read_b32 v85, v87
	ds_read_b32 v86, v88
	ds_read_b32 v87, v89
	ds_read_b32 v88, v90
	ds_read_b32 v89, v91
	ds_read_b32 v90, v92
	ds_read_b32 v91, v93
	ds_read_b32 v92, v94
	ds_read_b32 v93, v95
	ds_read_b32 v94, v139
	ds_read_b32 v95, v140
	s_waitcnt lgkmcnt(14)
; __device__ __forceinline__ void diff_tile(const bool near, const LAS unsigned char* Kb, const LAS unsigned char* Vb, const LAS float* btab, const LAS bf16x8* Qs, f32x16 (&O)[2][2],
;                                           float (&lsum)[2], int qpos, int k0, int l31, int hi, float c2, float farraw) {
;     ...
;             for (int r = 0; r < 16; ++r) { asm volatile("" : "+v"(bm[kb][r]));
;                 const int dist = qpos - (k0 + 32 * kb + (r & 3) + 8 * (r >> 2) + 4 * hi); bm[kb][r] = dist < 0 ? -INFINITY : (bm[kb][r] - farraw) * c2; }
	v_cmp_ge_i32_e32 vcc, v148, v96
	v_sub_f32_e32 v139, v141, v150
	v_mul_f32_e32 v139, 0x3e8293ee, v139
	v_sub_f32_e32 v140, v152, v150
	v_mul_f32_e32 v140, 0x3e8293ee, v140
	v_cndmask_b32_e32 v152, v219, v139, vcc
	v_cmp_lt_i32_e32 vcc, v96, v148
	v_pk_add_f32 v[66:67], v[66:67], v[150:151] neg_lo:[0,1] neg_hi:[0,1]
	s_nop 0
	v_cndmask_b32_e32 v153, v219, v140, vcc
	v_pk_mul_f32 v[66:67], v[66:67], s[92:93] op_sel_hi:[1,0]
	v_cmp_ge_i32_e32 vcc, v148, v110
	s_nop 1
	v_cndmask_b32_e32 v154, v219, v66, vcc
	v_cmp_ge_i32_e32 vcc, v147, v97
	s_nop 1
	v_cndmask_b32_e32 v155, v219, v67, vcc
	v_pk_add_f32 v[66:67], v[68:69], v[150:151] neg_lo:[0,1] neg_hi:[0,1]
	v_cmp_ge_i32_e32 vcc, v148, v112
	v_pk_mul_f32 v[66:67], v[66:67], s[92:93] op_sel_hi:[1,0]
	s_waitcnt lgkmcnt(13)
	s_waitcnt lgkmcnt(12)
	s_waitcnt lgkmcnt(11)
	s_waitcnt lgkmcnt(10)
	s_waitcnt lgkmcnt(9)
	v_cndmask_b32_e32 v156, v219, v66, vcc
	v_cmp_ge_i32_e32 vcc, v147, v111
	s_waitcnt lgkmcnt(8)
	s_waitcnt lgkmcnt(7)
	s_waitcnt lgkmcnt(6)
	s_waitcnt lgkmcnt(5)
	s_waitcnt lgkmcnt(4)
	v_cndmask_b32_e32 v157, v219, v67, vcc
	v_pk_add_f32 v[66:67], v[70:71], v[150:151] neg_lo:[0,1] neg_hi:[0,1]
	v_cmp_ge_i32_e32 vcc, v148, v114
	v_pk_mul_f32 v[66:67], v[66:67], s[92:93] op_sel_hi:[1,0]
	s_waitcnt lgkmcnt(3)
	s_waitcnt lgkmcnt(2)
	s_waitcnt lgkmcnt(1)
	s_waitcnt lgkmcnt(0)
	v_cndmask_b32_e32 v158, v219, v66, vcc
	v_cmp_ge_i32_e32 vcc, v147, v113
	s_nop 1
	v_cndmask_b32_e32 v159, v219, v67, vcc
	v_pk_add_f32 v[66:67], v[72:73], v[150:151] neg_lo:[0,1] neg_hi:[0,1]
	v_cmp_ge_i32_e32 vcc, v148, v116
	v_pk_mul_f32 v[66:67], v[66:67], s[92:93] op_sel_hi:[1,0]
	s_nop 0
	v_cndmask_b32_e32 v160, v219, v66, vcc
	v_cmp_ge_i32_e32 vcc, v147, v115
	s_nop 1
	v_cndmask_b32_e32 v161, v219, v67, vcc
	v_pk_add_f32 v[66:67], v[74:75], v[150:151] neg_lo:[0,1] neg_hi:[0,1]
	v_cmp_ge_i32_e32 vcc, v148, v118
	v_pk_mul_f32 v[66:67], v[66:67], s[92:93] op_sel_hi:[1,0]
	s_nop 0
	v_cndmask_b32_e32 v162, v219, v66, vcc
	v_cmp_ge_i32_e32 vcc, v147, v117
	s_nop 1
	v_cndmask_b32_e32 v163, v219, v67, vcc
	v_pk_add_f32 v[66:67], v[76:77], v[150:151] neg_lo:[0,1] neg_hi:[0,1]
	v_cmp_ge_i32_e32 vcc, v148, v120
	v_pk_mul_f32 v[66:67], v[66:67], s[92:93] op_sel_hi:[1,0]
	s_nop 0
	v_cndmask_b32_e32 v164, v219, v66, vcc
	v_cmp_ge_i32_e32 vcc, v147, v119
	s_nop 1
	v_cndmask_b32_e32 v165, v219, v67, vcc
	v_pk_add_f32 v[66:67], v[78:79], v[150:151] neg_lo:[0,1] neg_hi:[0,1]
	v_cmp_ge_i32_e32 vcc, v148, v122
	v_pk_mul_f32 v[66:67], v[66:67], s[92:93] op_sel_hi:[1,0]
	s_nop 0
	v_cndmask_b32_e32 v166, v219, v66, vcc
	v_cmp_ge_i32_e32 vcc, v147, v121
	s_nop 1
	v_cndmask_b32_e32 v167, v219, v67, vcc
	v_pk_add_f32 v[66:67], v[80:81], v[150:151] neg_lo:[0,1] neg_hi:[0,1]
	v_cmp_ge_i32_e32 vcc, v148, v124
	v_pk_mul_f32 v[66:67], v[66:67], s[92:93] op_sel_hi:[1,0]
	s_nop 0
	v_cndmask_b32_e32 v168, v219, v66, vcc
	v_cmp_ge_i32_e32 vcc, v147, v123
	s_nop 1
	v_cndmask_b32_e32 v169, v219, v67, vcc
	v_pk_add_f32 v[66:67], v[82:83], v[150:151] neg_lo:[0,1] neg_hi:[0,1]
	v_cmp_ge_i32_e32 vcc, v148, v126
	v_pk_mul_f32 v[66:67], v[66:67], s[92:93] op_sel_hi:[1,0]
	s_nop 0
	v_cndmask_b32_e32 v170, v219, v66, vcc
	v_cmp_ge_i32_e32 vcc, v147, v125
	s_nop 1
	v_cndmask_b32_e32 v171, v219, v67, vcc
	v_pk_add_f32 v[66:67], v[84:85], v[150:151] neg_lo:[0,1] neg_hi:[0,1]
	v_cmp_ge_i32_e32 vcc, v148, v128
	v_pk_mul_f32 v[66:67], v[66:67], s[92:93] op_sel_hi:[1,0]
	s_nop 0
	v_cndmask_b32_e32 v172, v219, v66, vcc
	v_cmp_ge_i32_e32 vcc, v147, v127
	s_nop 1
	v_cndmask_b32_e32 v173, v219, v67, vcc
	v_pk_add_f32 v[66:67], v[86:87], v[150:151] neg_lo:[0,1] neg_hi:[0,1]
	v_cmp_ge_i32_e32 vcc, v148, v130
	v_pk_mul_f32 v[66:67], v[66:67], s[92:93] op_sel_hi:[1,0]
	s_nop 0
	v_cndmask_b32_e32 v174, v219, v66, vcc
	v_cmp_ge_i32_e32 vcc, v147, v129
	s_nop 1
	v_cndmask_b32_e32 v175, v219, v67, vcc
	v_pk_add_f32 v[66:67], v[88:89], v[150:151] neg_lo:[0,1] neg_hi:[0,1]
	v_cmp_ge_i32_e32 vcc, v148, v132
	v_pk_mul_f32 v[66:67], v[66:67], s[92:93] op_sel_hi:[1,0]
	s_nop 0
	v_cndmask_b32_e32 v176, v219, v66, vcc
	v_cmp_ge_i32_e32 vcc, v147, v131
	s_nop 1
	v_cndmask_b32_e32 v177, v219, v67, vcc
	v_pk_add_f32 v[66:67], v[90:91], v[150:151] neg_lo:[0,1] neg_hi:[0,1]
	v_cmp_ge_i32_e32 vcc, v148, v134
	v_pk_mul_f32 v[66:67], v[66:67], s[92:93] op_sel_hi:[1,0]
	s_nop 0
	v_cndmask_b32_e32 v178, v219, v66, vcc
	v_cmp_ge_i32_e32 vcc, v147, v133
	s_nop 1
	v_cndmask_b32_e32 v179, v219, v67, vcc
	v_pk_add_f32 v[66:67], v[92:93], v[150:151] neg_lo:[0,1] neg_hi:[0,1]
	v_cmp_ge_i32_e32 vcc, v148, v136
	v_pk_mul_f32 v[66:67], v[66:67], s[92:93] op_sel_hi:[1,0]
	s_nop 0
	v_cndmask_b32_e32 v180, v219, v66, vcc
	v_cmp_ge_i32_e32 vcc, v147, v135
	s_nop 1
	v_cndmask_b32_e32 v181, v219, v67, vcc
	v_pk_add_f32 v[66:67], v[94:95], v[150:151] neg_lo:[0,1] neg_hi:[0,1]
	v_cmp_ge_i32_e32 vcc, v148, v138
	v_pk_mul_f32 v[66:67], v[66:67], s[92:93] op_sel_hi:[1,0]
	s_nop 0
	v_cndmask_b32_e32 v182, v219, v66, vcc
	v_cmp_ge_i32_e32 vcc, v147, v137
	s_nop 1
	v_cndmask_b32_e32 v183, v219, v67, vcc
